# speedup vs baseline: 1.0220x; 1.0108x over previous
.LBB2_365:
	s_or_b64 exec, exec, s[6:7]
	s_load_dwordx2 s[12:13], s[0:1], 0x18
	s_lshl_b64 s[10:11], s[2:3], 10
	v_cmp_gt_i32_e32 vcc, s22, v0
	s_waitcnt lgkmcnt(0)
	s_barrier
	s_cmp_gt_i32 s22, 16
	s_cbranch_scc1 .Lrank1_slow
	v_lshrrev_b32_e32 v2, 4, v0
	v_and_b32_e32 v3, 15, v0
	v_lshlrev_b32_e32 v4, 3, v2
	v_lshlrev_b32_e32 v5, 3, v3
	ds_read_b64 v[6:7], v4
	ds_read_b64 v[8:9], v5
	v_lshlrev_b32_e32 v4, 2, v2
	v_lshlrev_b32_e32 v5, 2, v3
	ds_read_b32 v10, v4 offset:3072
	ds_read_b32 v11, v5 offset:3072
	v_and_b32_e32 v12, 63, v0
	v_lshrrev_b32_e32 v12, 4, v12
	s_waitcnt lgkmcnt(0)
	v_cmp_gt_f64_e64 s[0:1], v[8:9], v[6:7]
	v_cmp_eq_f64_e64 s[2:3], v[8:9], v[6:7]
	v_cmp_lt_i32_e64 s[4:5], v11, v10
	v_cmp_gt_i32_e64 s[18:19], s22, v3
	s_and_b64 s[2:3], s[2:3], s[4:5]
	s_or_b64 s[0:1], s[0:1], s[2:3]
	s_and_b64 s[0:1], s[0:1], s[18:19]
	v_mov_b32_e32 v13, s0
	v_mov_b32_e32 v14, s1
	v_cmp_lt_u32_e64 s[2:3], 1, v12
	v_and_b32_e32 v12, 1, v12
	v_lshlrev_b32_e32 v12, 4, v12
	v_cndmask_b32_e64 v13, v13, v14, s[2:3]
	v_lshrrev_b32_e32 v13, v12, v13
	v_and_b32_e32 v13, 0xffff, v13
	v_bcnt_u32_b32 v13, v13, 0
	v_cmp_gt_i32_e64 s[2:3], s22, v2
	v_cmp_eq_u32_e64 s[4:5], 0, v3
	s_and_b64 s[2:3], s[2:3], s[4:5]
	v_cmp_eq_u32_e64 s[0:1], 3, v13
	s_and_b64 s[0:1], s[0:1], s[2:3]
	s_mov_b64 s[16:17], exec
	s_and_b64 exec, exec, s[0:1]
	v_mov_b32_e32 v12, 0
	ds_write_b64 v12, v[6:7] offset:6736
	s_branch .LBB2_395
.Lrank1_slow:
	s_and_saveexec_b64 s[16:17], vcc
	s_cbranch_execz .LBB2_395
	s_add_i32 s0, s22, -1
	s_and_b32 s23, s22, 7
	s_cmp_gt_u32 s0, 6
	s_cselect_b64 s[0:1], -1, 0
	s_and_b32 s24, s22, -8
	s_cmp_lg_u32 s23, 0
	v_cndmask_b32_e64 v2, 0, 1, s[0:1]
	s_cselect_b64 s[2:3], -1, 0
	v_cmp_ne_u32_e64 s[0:1], 1, v2
	v_cndmask_b32_e64 v2, 0, 1, s[2:3]
	s_mov_b64 s[18:19], 0
	v_cmp_ne_u32_e64 s[2:3], 1, v2
	v_mov_b32_e32 v6, 0
	v_mov_b32_e32 v7, v0
	s_branch .LBB2_368

.LBB2_410:
	s_or_b64 exec, exec, s[0:1]
	v_cmp_gt_i32_e32 vcc, s18, v0
	s_waitcnt lgkmcnt(0)
	s_barrier
	s_cmp_gt_i32 s18, 16
	s_cbranch_scc1 .Lrank2_slow
	v_lshrrev_b32_e32 v2, 4, v0
	v_and_b32_e32 v3, 15, v0
	v_lshlrev_b32_e32 v4, 3, v2
	v_lshlrev_b32_e32 v5, 3, v3
	ds_read_b64 v[6:7], v4
	ds_read_b64 v[8:9], v5
	v_lshlrev_b32_e32 v4, 2, v2
	v_lshlrev_b32_e32 v5, 2, v3
	ds_read_b32 v10, v4 offset:3072
	ds_read_b32 v11, v5 offset:3072
	v_and_b32_e32 v12, 63, v0
	v_lshrrev_b32_e32 v12, 4, v12
	s_waitcnt lgkmcnt(0)
	v_cmp_gt_f64_e64 s[0:1], v[8:9], v[6:7]
	v_cmp_eq_f64_e64 s[2:3], v[8:9], v[6:7]
	v_cmp_lt_i32_e64 s[4:5], v11, v10
	v_cmp_gt_i32_e64 s[14:15], s18, v3
	s_and_b64 s[2:3], s[2:3], s[4:5]
	s_or_b64 s[0:1], s[0:1], s[2:3]
	s_and_b64 s[0:1], s[0:1], s[14:15]
	v_mov_b32_e32 v13, s0
	v_mov_b32_e32 v14, s1
	v_cmp_lt_u32_e64 s[2:3], 1, v12
	v_and_b32_e32 v12, 1, v12
	v_lshlrev_b32_e32 v12, 4, v12
	v_cndmask_b32_e64 v13, v13, v14, s[2:3]
	v_lshrrev_b32_e32 v13, v12, v13
	v_and_b32_e32 v13, 0xffff, v13
	v_bcnt_u32_b32 v13, v13, 0
	v_cmp_gt_i32_e64 s[2:3], s18, v2
	v_cmp_eq_u32_e64 s[4:5], 0, v3
	s_and_b64 s[2:3], s[2:3], s[4:5]
	v_cmp_gt_u32_e64 s[0:1], 4, v13
	s_and_b64 s[0:1], s[0:1], s[2:3]
	s_mov_b64 s[6:7], exec
	s_and_b64 exec, exec, s[0:1]
	v_lshlrev_b32_e32 v12, 2, v13
	ds_write_b32 v12, v10 offset:6720
	s_branch .LBB2_440
.Lrank2_slow:
	s_and_saveexec_b64 s[6:7], vcc
	s_cbranch_execz .LBB2_440
	s_add_i32 s0, s18, -1
	s_and_b32 s19, s18, 7
	s_cmp_gt_u32 s0, 6
	s_cselect_b64 s[0:1], -1, 0
	s_and_b32 s20, s18, -8
	s_cmp_lg_u32 s19, 0
	v_cndmask_b32_e64 v2, 0, 1, s[0:1]
	s_cselect_b64 s[2:3], -1, 0
	v_cmp_ne_u32_e64 s[0:1], 1, v2
	v_cndmask_b32_e64 v2, 0, 1, s[2:3]
	s_mov_b64 s[14:15], 0
	v_cmp_ne_u32_e64 s[2:3], 1, v2
	s_branch .LBB2_413
